# speedup vs baseline: 1.0204x; 1.0204x over previous
.LBB1_12:
	s_mov_b32 s0, s44
	s_add_i32 s44, s44, 1
	s_cmp_ge_u32 s44, s42
	s_cselect_b64 s[22:23], -1, 0
	s_cmp_lt_u32 s44, s42
	s_cselect_b32 s2, s44, s0
	s_waitcnt vmcnt(0)
	s_lshl_b32 s0, s2, 4
	s_mov_b32 s1, s17
	s_mov_b32 m0, s43
	ds_read_b128 v[76:79], v119 offset:32768
	ds_read_b128 v[80:83], v119 offset:36864
	ds_read_b128 v[84:87], v120 offset:32768
	ds_read_b128 v[88:91], v120 offset:36864
	ds_read_b128 v[92:95], v121
	ds_read_b128 v[96:99], v121 offset:4096
	ds_read_b128 v[128:131], v122
	ds_read_b128 v[132:135], v122 offset:4096
	ds_read_b128 v[72:75], v123
	s_waitcnt lgkmcnt(0)
	v_lshl_add_u64 v[70:71], s[0:1], 2, v[2:3]
	global_load_lds_dword v[70:71], off
	ds_read_b128 v[156:159], v115
	ds_read_b128 v[160:163], v115 offset:1024
	ds_read_b128 v[164:167], v115 offset:2048
	v_cvt_pk_bf16_f32 v136, v76, v77
	v_cvt_pk_bf16_f32 v137, v78, v79
	v_cvt_pk_bf16_f32 v138, v84, v85
	v_cvt_pk_bf16_f32 v139, v86, v87
	v_cvt_pk_bf16_f32 v140, v92, v93
	v_cvt_pk_bf16_f32 v141, v94, v95
	v_cvt_pk_bf16_f32 v142, v128, v129
	v_cvt_pk_bf16_f32 v143, v130, v131
	v_cvt_pk_bf16_f32 v144, v80, v81
	v_cvt_pk_bf16_f32 v145, v82, v83
	v_cvt_pk_bf16_f32 v146, v88, v89
	v_cvt_pk_bf16_f32 v147, v90, v91
	v_cvt_pk_bf16_f32 v128, v96, v97
	v_cvt_pk_bf16_f32 v129, v98, v99
	v_cvt_pk_bf16_f32 v130, v132, v133
	v_cvt_pk_bf16_f32 v131, v134, v135
	s_lshl_b32 s0, s2, 13
	s_cmp_lt_u32 s44, s42
	s_cselect_b32 s0, s0, 0x1e848000
	s_mov_b32 s61, s0
	ds_read_b128 v[132:135], v115 offset:3072
	s_waitcnt lgkmcnt(3)
	v_mfma_f32_16x16x32_bf16 v[148:151], v[136:139], v[156:159], v[36:39]
	ds_read_b128 v[156:159], v115 offset:4096
	s_waitcnt lgkmcnt(3)
	v_mfma_f32_16x16x32_bf16 v[152:155], v[136:139], v[160:163], v[40:43]
	ds_read_b128 v[160:163], v115 offset:5120
	s_waitcnt lgkmcnt(3)
	v_mfma_f32_16x16x32_bf16 v[96:99], v[136:139], v[164:167], v[44:47]
	ds_read_b128 v[164:167], v115 offset:6144
	s_waitcnt lgkmcnt(3)
	v_mfma_f32_16x16x32_bf16 v[92:95], v[136:139], v[132:135], v[48:51]
	ds_read_b128 v[132:135], v115 offset:7168
	s_waitcnt lgkmcnt(3)
	v_mfma_f32_16x16x32_bf16 v[88:91], v[136:139], v[156:159], v[52:55]
	ds_read_b128 v[156:159], v115 offset:8192
	s_waitcnt lgkmcnt(3)
	v_mfma_f32_16x16x32_bf16 v[84:87], v[136:139], v[160:163], v[56:59]
	ds_read_b128 v[160:163], v115 offset:9216
	s_waitcnt lgkmcnt(3)
	v_mfma_f32_16x16x32_bf16 v[80:83], v[136:139], v[164:167], v[60:63]
	ds_read_b128 v[164:167], v115 offset:10240
	s_waitcnt lgkmcnt(3)
	v_mfma_f32_16x16x32_bf16 v[76:79], v[136:139], v[132:135], v[64:67]
	s_mov_b32 m0, s47
	s_nop 0
	buffer_load_dwordx4 v113, s[12:15], s61 offen nt lds
	ds_read_b128 v[132:135], v115 offset:11264
	s_waitcnt lgkmcnt(3)
	v_mfma_f32_16x16x32_bf16 v[148:151], v[140:143], v[156:159], v[148:151]
	ds_read_b128 v[156:159], v115 offset:12288
	s_waitcnt lgkmcnt(3)
	v_mfma_f32_16x16x32_bf16 v[152:155], v[140:143], v[160:163], v[152:155]
	ds_read_b128 v[160:163], v115 offset:13312
	s_waitcnt lgkmcnt(3)
	v_mfma_f32_16x16x32_bf16 v[96:99], v[140:143], v[164:167], v[96:99]
	ds_read_b128 v[164:167], v115 offset:14336
	s_waitcnt lgkmcnt(3)
	v_mfma_f32_16x16x32_bf16 v[92:95], v[140:143], v[132:135], v[92:95]
	ds_read_b128 v[132:135], v115 offset:15360
	s_waitcnt lgkmcnt(3)
	v_mfma_f32_16x16x32_bf16 v[88:91], v[140:143], v[156:159], v[88:91]
	ds_read_b128 v[156:159], v115 offset:16384
	s_waitcnt lgkmcnt(3)
	v_mfma_f32_16x16x32_bf16 v[84:87], v[140:143], v[160:163], v[84:87]
	ds_read_b128 v[160:163], v115 offset:17408
	s_waitcnt lgkmcnt(3)
	v_mfma_f32_16x16x32_bf16 v[80:83], v[140:143], v[164:167], v[80:83]
	ds_read_b128 v[164:167], v115 offset:18432
	s_waitcnt lgkmcnt(3)
	v_mfma_f32_16x16x32_bf16 v[76:79], v[140:143], v[132:135], v[76:79]
	s_or_b32 s62, s61, 0x800
	s_mov_b32 m0, s48
	s_nop 0
	buffer_load_dwordx4 v113, s[12:15], s62 offen nt lds
	ds_read_b128 v[132:135], v115 offset:19456
	s_waitcnt lgkmcnt(3)
	v_mfma_f32_16x16x32_bf16 v[148:151], v[144:147], v[156:159], v[148:151]
	ds_read_b128 v[156:159], v115 offset:20480
	s_waitcnt lgkmcnt(3)
	v_mfma_f32_16x16x32_bf16 v[152:155], v[144:147], v[160:163], v[152:155]
	ds_read_b128 v[160:163], v115 offset:21504
	s_waitcnt lgkmcnt(3)
	v_mfma_f32_16x16x32_bf16 v[96:99], v[144:147], v[164:167], v[96:99]
	ds_read_b128 v[164:167], v115 offset:22528
	s_waitcnt lgkmcnt(3)
	v_mfma_f32_16x16x32_bf16 v[92:95], v[144:147], v[132:135], v[92:95]
	ds_read_b128 v[132:135], v115 offset:23552
	s_waitcnt lgkmcnt(3)
	v_mfma_f32_16x16x32_bf16 v[88:91], v[144:147], v[156:159], v[88:91]
	ds_read_b128 v[156:159], v115 offset:24576
	s_waitcnt lgkmcnt(3)
	v_mfma_f32_16x16x32_bf16 v[84:87], v[144:147], v[160:163], v[84:87]
	ds_read_b128 v[160:163], v115 offset:25600
	s_waitcnt lgkmcnt(3)
	v_mfma_f32_16x16x32_bf16 v[80:83], v[144:147], v[164:167], v[80:83]
	ds_read_b128 v[164:167], v115 offset:26624
	s_waitcnt lgkmcnt(3)
	v_mfma_f32_16x16x32_bf16 v[76:79], v[144:147], v[132:135], v[76:79]
	s_or_b32 s62, s61, 0x1000
	s_mov_b32 m0, s49
	s_nop 0
	buffer_load_dwordx4 v113, s[12:15], s62 offen nt lds
	ds_read_b128 v[132:135], v115 offset:27648
	s_waitcnt lgkmcnt(3)
	v_mfma_f32_16x16x32_bf16 v[148:151], v[128:131], v[156:159], v[148:151]
	ds_read_b128 v[156:159], v115 offset:28672
	s_waitcnt lgkmcnt(3)
	v_mfma_f32_16x16x32_bf16 v[152:155], v[128:131], v[160:163], v[152:155]
	ds_read_b128 v[160:163], v115 offset:29696
	s_waitcnt lgkmcnt(3)
	v_mfma_f32_16x16x32_bf16 v[96:99], v[128:131], v[164:167], v[96:99]
	ds_read_b128 v[164:167], v115 offset:30720
	s_waitcnt lgkmcnt(3)
	v_mfma_f32_16x16x32_bf16 v[92:95], v[128:131], v[132:135], v[92:95]
	ds_read_b128 v[132:135], v115 offset:31744
	s_waitcnt lgkmcnt(3)
	v_mfma_f32_16x16x32_bf16 v[88:91], v[128:131], v[156:159], v[88:91]
	s_waitcnt lgkmcnt(2)
	v_mfma_f32_16x16x32_bf16 v[84:87], v[128:131], v[160:163], v[84:87]
	s_waitcnt lgkmcnt(1)
	v_mfma_f32_16x16x32_bf16 v[80:83], v[128:131], v[164:167], v[80:83]
	s_waitcnt lgkmcnt(0)
	v_mfma_f32_16x16x32_bf16 v[76:79], v[128:131], v[132:135], v[76:79]
	s_or_b32 s62, s61, 0x1800
	s_mov_b32 m0, s50
	s_nop 0
	buffer_load_dwordx4 v113, s[12:15], s62 offen nt lds
	ds_read2_b32 v[136:137], v114 offset0:128 offset1:144
	ds_read2_b32 v[138:139], v125 offset1:16
	ds_read2_b32 v[140:141], v114 offset0:160 offset1:176
	ds_read2_b32 v[142:143], v125 offset0:32 offset1:48
	ds_read2_b32 v[144:145], v114 offset0:192 offset1:208
	ds_read2_b32 v[146:147], v125 offset0:64 offset1:80
	ds_read2_b32 v[156:157], v114 offset0:224 offset1:240
	ds_read2_b32 v[158:159], v125 offset0:96 offset1:112
	v_fma_f32 v70, v149, v149, 0
	v_fmac_f32_e32 v70, v153, v153
	v_fmac_f32_e32 v70, v97, v97
	v_fmac_f32_e32 v70, v93, v93
	v_fmac_f32_e32 v70, v89, v89
	v_fmac_f32_e32 v70, v85, v85
	v_fmac_f32_e32 v70, v81, v81
	v_fmac_f32_e32 v70, v77, v77
	v_fma_f32 v68, v148, v148, 0
	v_fmac_f32_e32 v68, v152, v152
	v_add_f32_dpp v70, v70, v70 quad_perm:[1,0,3,2] row_mask:0xf bank_mask:0xf bound_ctrl:1
	v_fmac_f32_e32 v68, v96, v96
	v_fmac_f32_e32 v68, v92, v92
	v_add_f32_dpp v70, v70, v70 quad_perm:[2,3,0,1] row_mask:0xf bank_mask:0xf bound_ctrl:1
	v_fmac_f32_e32 v68, v88, v88
	v_fmac_f32_e32 v68, v84, v84
	v_add_f32_dpp v70, v70, v70 row_half_mirror row_mask:0xf bank_mask:0xf bound_ctrl:1
	v_fmac_f32_e32 v68, v80, v80
	v_fmac_f32_e32 v68, v76, v76
	v_add_f32_dpp v70, v70, v70 row_mirror row_mask:0xf bank_mask:0xf bound_ctrl:1
	v_fmamk_f32 v70, v70, 0x3c000000, v124
	v_rsq_f32_e32 v127, v70
	v_fma_f32 v70, v150, v150, 0
	v_fmac_f32_e32 v70, v154, v154
	v_fmac_f32_e32 v70, v98, v98
	v_fmac_f32_e32 v70, v94, v94
	v_fmac_f32_e32 v70, v90, v90
	v_fmac_f32_e32 v70, v86, v86
	v_fmac_f32_e32 v70, v82, v82
	v_fmac_f32_e32 v70, v78, v78
	v_add_f32_dpp v68, v68, v68 quad_perm:[1,0,3,2] row_mask:0xf bank_mask:0xf bound_ctrl:1
	v_mul_f32_e32 v131, v127, v149
	v_add_f32_dpp v70, v70, v70 quad_perm:[1,0,3,2] row_mask:0xf bank_mask:0xf bound_ctrl:1
	v_add_f32_dpp v68, v68, v68 quad_perm:[2,3,0,1] row_mask:0xf bank_mask:0xf bound_ctrl:1
	v_mul_f32_e32 v81, v127, v81
	v_add_f32_dpp v70, v70, v70 quad_perm:[2,3,0,1] row_mask:0xf bank_mask:0xf bound_ctrl:1
	v_add_f32_dpp v68, v68, v68 row_half_mirror row_mask:0xf bank_mask:0xf bound_ctrl:1
	v_cmp_gt_u32_e64 s[0:1], s55, v72
	v_add_f32_dpp v70, v70, v70 row_half_mirror row_mask:0xf bank_mask:0xf bound_ctrl:1
	v_add_f32_dpp v68, v68, v68 row_mirror row_mask:0xf bank_mask:0xf bound_ctrl:1
	v_fmamk_f32 v68, v68, 0x3c000000, v124
	v_add_f32_dpp v70, v70, v70 row_mirror row_mask:0xf bank_mask:0xf bound_ctrl:1
	v_fmamk_f32 v70, v70, 0x3c000000, v124
	v_rsq_f32_e32 v130, v70
	v_fma_f32 v70, v151, v151, 0
	v_fmac_f32_e32 v70, v155, v155
	v_fmac_f32_e32 v70, v99, v99
	v_fmac_f32_e32 v70, v95, v95
	v_fmac_f32_e32 v70, v91, v91
	v_fmac_f32_e32 v70, v87, v87
	v_fmac_f32_e32 v70, v83, v83
	v_fmac_f32_e32 v70, v79, v79
	v_rsq_f32_e32 v68, v68
	v_mul_f32_e32 v98, v130, v98
	v_add_f32_dpp v70, v70, v70 quad_perm:[1,0,3,2] row_mask:0xf bank_mask:0xf bound_ctrl:1
	v_mul_f32_e32 v90, v130, v90
	v_mul_f32_e32 v111, v68, v148
	v_add_f32_dpp v110, v70, v70 quad_perm:[2,3,0,1] row_mask:0xf bank_mask:0xf bound_ctrl:1
	s_nop 1
	v_add_f32_dpp v110, v110, v110 row_half_mirror row_mask:0xf bank_mask:0xf bound_ctrl:1
	v_mul_f32_e32 v96, v68, v96
	v_mul_f32_e32 v92, v68, v92
	v_add_f32_dpp v110, v110, v110 row_mirror row_mask:0xf bank_mask:0xf bound_ctrl:1
	v_fmamk_f32 v110, v110, 0x3c000000, v124
	s_waitcnt lgkmcnt(0)
	s_or_b32 s62, s61, 0x100
	s_mov_b32 m0, s51
	s_nop 0
	buffer_load_dwordx4 v113, s[12:15], s62 offen nt lds
	v_fma_f32 v111, v111, v136, v138
	v_fma_f32 v131, v131, v136, v138
	v_exp_f32_e32 v111, v111
	v_exp_f32_e32 v131, v131
	v_rsq_f32_e32 v132, v110
	v_mul_f32_e32 v88, v68, v88
	v_add_f32_e32 v110, 1.0, v111
	v_add_f32_e32 v111, 1.0, v131
	v_mul_f32_e32 v131, v130, v150
	v_mul_f32_e32 v133, v132, v151
	v_fma_f32 v131, v131, v136, v138
	v_fma_f32 v70, v133, v136, v138
	v_exp_f32_e32 v131, v131
	v_exp_f32_e32 v70, v70
	v_rcp_f32_e32 v110, v110
	v_rcp_f32_e32 v111, v111
	v_add_f32_e32 v128, 1.0, v131
	v_add_f32_e32 v70, 1.0, v70
	v_rcp_f32_e32 v128, v128
	v_rcp_f32_e32 v70, v70
	v_mul_f32_e32 v131, v68, v152
	v_fma_f32 v131, v131, v137, v139
	v_cvt_pk_bf16_f32 v110, v110, v111
	v_cvt_pk_bf16_f32 v111, v128, v70
	v_mul_f32_e32 v128, v127, v153
	v_exp_f32_e32 v131, v131
	v_fma_f32 v128, v128, v137, v139
	v_exp_f32_e32 v128, v128
	v_mul_f32_e32 v99, v132, v99
	v_add_f32_e32 v70, 1.0, v131
	v_rcp_f32_e32 v133, v70
	v_add_f32_e32 v70, 1.0, v128
	v_mul_f32_e32 v131, v130, v154
	v_rcp_f32_e32 v134, v70
	v_mul_f32_e32 v70, v132, v155
	v_fma_f32 v131, v131, v137, v139
	v_fma_f32 v129, v70, v137, v139
	v_exp_f32_e32 v135, v129
	v_exp_f32_e32 v131, v131
	v_mul_f32_e32 v91, v132, v91
	v_add_f32_e32 v135, 1.0, v135
	v_rcp_f32_e32 v135, v135
	s_or_b32 s62, s61, 0x900
	s_mov_b32 m0, s52
	s_nop 0
	buffer_load_dwordx4 v113, s[12:15], s62 offen nt lds
	v_fma_f32 v96, v96, v140, v142
	v_exp_f32_e32 v136, v96
	v_mul_f32_e32 v96, v127, v97
	v_fma_f32 v96, v96, v140, v142
	v_exp_f32_e32 v97, v96
	v_fma_f32 v98, v98, v140, v142
	v_fma_f32 v70, v99, v140, v142
	v_exp_f32_e32 v98, v98
	v_exp_f32_e32 v70, v70
	v_add_f32_e32 v97, 1.0, v97
	v_cvt_pk_bf16_f32 v96, v133, v134
	v_add_f32_e32 v133, 1.0, v136
	v_rcp_f32_e32 v99, v97
	v_add_f32_e32 v97, 1.0, v98
	v_add_f32_e32 v70, 1.0, v70
	v_fma_f32 v92, v92, v141, v143
	v_rcp_f32_e32 v133, v133
	v_rcp_f32_e32 v128, v97
	v_rcp_f32_e32 v70, v70
	v_exp_f32_e32 v92, v92
	v_cvt_pk_bf16_f32 v98, v133, v99
	v_add_f32_e32 v131, 1.0, v131
	v_cvt_pk_bf16_f32 v99, v128, v70
	v_add_f32_e32 v70, 1.0, v92
	v_mul_f32_e32 v92, v127, v93
	v_fma_f32 v92, v92, v141, v143
	v_exp_f32_e32 v92, v92
	v_mul_f32_e32 v93, v130, v94
	v_fma_f32 v93, v93, v141, v143
	v_rcp_f32_e32 v131, v131
	v_exp_f32_e32 v93, v93
	v_rcp_f32_e32 v94, v70
	v_add_f32_e32 v70, 1.0, v92
	v_rcp_f32_e32 v128, v70
	v_mul_f32_e32 v70, v132, v95
	v_cvt_pk_bf16_f32 v97, v131, v135
	v_add_f32_e32 v131, 1.0, v93
	v_fma_f32 v129, v70, v141, v143
	v_exp_f32_e32 v95, v129
	v_rcp_f32_e32 v129, v131
	v_mul_f32_e32 v84, v68, v84
	v_mul_f32_e32 v80, v68, v80
	s_or_b32 s62, s61, 0x1100
	s_mov_b32 m0, s53
	s_nop 0
	buffer_load_dwordx4 v113, s[12:15], s62 offen nt lds
	v_fma_f32 v88, v88, v144, v146
	v_exp_f32_e32 v131, v88
	v_mul_f32_e32 v88, v127, v89
	v_fma_f32 v88, v88, v144, v146
	v_exp_f32_e32 v89, v88
	v_fma_f32 v90, v90, v144, v146
	v_fma_f32 v70, v91, v144, v146
	v_exp_f32_e32 v90, v90
	v_exp_f32_e32 v70, v70
	v_add_f32_e32 v89, 1.0, v89
	v_cvt_pk_bf16_f32 v88, v94, v128
	v_add_f32_e32 v94, 1.0, v131
	v_rcp_f32_e32 v91, v89
	v_add_f32_e32 v89, 1.0, v90
	v_add_f32_e32 v70, 1.0, v70
	v_fma_f32 v84, v84, v145, v147
	v_rcp_f32_e32 v94, v94
	v_rcp_f32_e32 v92, v89
	v_rcp_f32_e32 v70, v70
	v_exp_f32_e32 v84, v84
	v_cvt_pk_bf16_f32 v90, v94, v91
	v_mul_f32_e32 v68, v68, v76
	v_cvt_pk_bf16_f32 v91, v92, v70
	v_add_f32_e32 v70, 1.0, v84
	v_mul_f32_e32 v84, v127, v85
	v_fma_f32 v84, v84, v145, v147
	v_mul_f32_e32 v85, v130, v86
	v_exp_f32_e32 v84, v84
	v_fma_f32 v85, v85, v145, v147
	v_exp_f32_e32 v85, v85
	v_rcp_f32_e32 v92, v70
	v_add_f32_e32 v70, 1.0, v84
	v_rcp_f32_e32 v84, v70
	v_add_f32_e32 v70, 1.0, v85
	v_mul_f32_e32 v85, v132, v87
	v_fma_f32 v93, v85, v145, v147
	v_exp_f32_e32 v85, v93
	v_rcp_f32_e32 v93, v70
	v_mul_f32_e32 v76, v127, v77
	v_mul_f32_e32 v82, v130, v82
	v_mul_f32_e32 v83, v132, v83
	v_mul_f32_e32 v77, v130, v78
	s_or_b32 s62, s61, 0x1900
	s_mov_b32 m0, s54
	s_nop 0
	buffer_load_dwordx4 v113, s[12:15], s62 offen nt lds
	v_fma_f32 v76, v76, v157, v159
	v_mul_f32_e32 v78, v132, v79
	v_fma_f32 v80, v80, v156, v158
	v_fma_f32 v81, v81, v156, v158
	v_fma_f32 v82, v82, v156, v158
	v_fma_f32 v70, v83, v156, v158
	v_fma_f32 v68, v68, v157, v159
	v_exp_f32_e32 v76, v76
	v_fma_f32 v77, v77, v157, v159
	v_fma_f32 v87, v78, v157, v159
	v_exp_f32_e32 v82, v82
	v_exp_f32_e32 v70, v70
	v_exp_f32_e32 v68, v68
	v_exp_f32_e32 v77, v77
	v_exp_f32_e32 v71, v87
	v_add_f32_e32 v76, 1.0, v76
	v_add_f32_e32 v82, 1.0, v82
	v_add_f32_e32 v70, 1.0, v70
	v_add_f32_e32 v68, 1.0, v68
	v_rcp_f32_e32 v78, v76
	v_add_f32_e32 v76, 1.0, v77
	v_add_f32_e32 v71, 1.0, v71
	v_rcp_f32_e32 v82, v82
	v_rcp_f32_e32 v70, v70
	v_rcp_f32_e32 v68, v68
	v_rcp_f32_e32 v79, v76
	v_rcp_f32_e32 v71, v71
	v_exp_f32_e32 v80, v80
	v_exp_f32_e32 v81, v81
	v_cvt_pk_bf16_f32 v77, v82, v70
	v_cvt_pk_bf16_f32 v78, v68, v78
	v_cvt_pk_bf16_f32 v79, v79, v71
	v_subrev_u32_e32 v68, s16, v72
	v_subrev_u32_e32 v70, s16, v73
	v_subrev_u32_e32 v71, s16, v74
	v_add_f32_e32 v95, 1.0, v95
	v_add_f32_e32 v85, 1.0, v85
	v_add_f32_e32 v80, 1.0, v80
	v_add_f32_e32 v81, 1.0, v81
	v_max3_u32 v68, v68, v70, v71
	v_subrev_u32_e32 v70, s16, v75
	v_rcp_f32_e32 v95, v95
	v_rcp_f32_e32 v85, v85
	v_rcp_f32_e32 v80, v80
	v_rcp_f32_e32 v81, v81
	v_max_u32_e32 v68, v68, v70
	v_cmp_gt_u32_e32 vcc, 16, v68
	s_cmp_eq_u64 vcc, -1
	s_cselect_b64 s[24:25], -1, 0
	s_cmp_lg_u64 vcc, -1
	v_cvt_pk_bf16_f32 v89, v129, v95
	v_cvt_pk_bf16_f32 v84, v92, v84
	v_cvt_pk_bf16_f32 v85, v93, v85
	v_cvt_pk_bf16_f32 v76, v80, v81
	s_cselect_b64 s[26:27], -1, 0
	v_cmp_gt_u32_e64 s[2:3], s55, v73
	v_cmp_gt_u32_e64 s[4:5], s55, v74
	v_cmp_gt_u32_e64 s[6:7], s55, v75
	s_mov_b32 s8, 0
	s_branch .LBB1_14
